# grid barriers: waiting workgroups poll the top-level generation word directly (one polling stage instead of two)
# speedup vs baseline: 1.0089x; 1.0089x over previous
.LBB0_123:
	s_or_b64 exec, exec, s[8:9]
	v_cvt_f32_u32_e32 v5, v3
	s_waitcnt vmcnt(0)
	v_readfirstlane_b32 s6, v4
	v_sub_u32_e32 v4, 0, v3
	v_rcp_iflag_f32_e32 v5, v5
	v_add_u32_e32 v6, s6, v2
	v_mul_f32_e32 v5, 0x4f7ffffe, v5
	v_cvt_u32_f32_e32 v5, v5
	v_mul_lo_u32 v2, v4, v5
	v_mul_hi_u32 v2, v5, v2
	v_add_u32_e32 v2, v5, v2
	v_mul_hi_u32 v2, v6, v2
	v_mul_lo_u32 v4, v2, v3
	v_sub_u32_e32 v4, v6, v4
	v_add_u32_e32 v5, 1, v2
	v_cmp_ge_u32_e32 vcc, v4, v3
	s_nop 1
	v_cndmask_b32_e32 v2, v2, v5, vcc
	v_sub_u32_e32 v5, v4, v3
	v_cndmask_b32_e32 v4, v4, v5, vcc
	v_add_u32_e32 v5, 1, v2
	v_cmp_ge_u32_e32 vcc, v4, v3
	v_add_u32_e32 v4, 1, v6
	s_nop 0
	v_cndmask_b32_e32 v2, v2, v5, vcc
	v_mul_lo_u32 v5, v3, v2
	v_add_u32_e32 v3, v5, v3
	v_cmp_ne_u32_e32 vcc, v4, v3
	s_and_saveexec_b64 s[6:7], vcc
	s_xor_b64 s[6:7], exec, s[6:7]
	s_cbranch_execz .LBB0_137
	s_waitcnt lgkmcnt(0)
	v_readlane_b32 s12, v243, 7
	v_readlane_b32 s13, v243, 8
	v_mov_b32_e32 v1, 0
	s_add_u32 s12, s12, 0x3500
	s_addc_u32 s13, s13, 0
	global_load_dword v1, v1, s[12:13] sc1
	s_waitcnt vmcnt(0)
	v_cmp_eq_u32_e32 vcc, v1, v2
	s_and_saveexec_b64 s[8:9], vcc
	s_cbranch_execz .LBB0_136
	s_load_dwordx4 s[16:19], s[96:97], 0xb8
	s_mov_b32 s24, 1
	s_mov_b64 s[14:15], 0
	v_mov_b32_e32 v1, 0
	s_waitcnt lgkmcnt(0)
	s_add_u32 s10, s16, 0x4200
	s_addc_u32 s11, s17, 0
	s_branch .LBB0_127

.LBB0_864:
	s_or_b64 exec, exec, s[8:9]
	v_cvt_f32_u32_e32 v5, v3
	s_waitcnt vmcnt(0)
	v_readfirstlane_b32 s6, v4
	v_sub_u32_e32 v4, 0, v3
	v_rcp_iflag_f32_e32 v5, v5
	v_add_u32_e32 v6, s6, v2
	v_mul_f32_e32 v5, 0x4f7ffffe, v5
	v_cvt_u32_f32_e32 v5, v5
	v_mul_lo_u32 v2, v4, v5
	v_mul_hi_u32 v2, v5, v2
	v_add_u32_e32 v2, v5, v2
	v_mul_hi_u32 v2, v6, v2
	v_mul_lo_u32 v4, v2, v3
	v_sub_u32_e32 v4, v6, v4
	v_add_u32_e32 v5, 1, v2
	v_cmp_ge_u32_e32 vcc, v4, v3
	s_nop 1
	v_cndmask_b32_e32 v2, v2, v5, vcc
	v_sub_u32_e32 v5, v4, v3
	v_cndmask_b32_e32 v4, v4, v5, vcc
	v_add_u32_e32 v5, 1, v2
	v_cmp_ge_u32_e32 vcc, v4, v3
	v_add_u32_e32 v4, 1, v6
	s_nop 0
	v_cndmask_b32_e32 v2, v2, v5, vcc
	v_mul_lo_u32 v5, v3, v2
	v_add_u32_e32 v3, v5, v3
	v_cmp_ne_u32_e32 vcc, v4, v3
	s_and_saveexec_b64 s[6:7], vcc
	s_xor_b64 s[6:7], exec, s[6:7]
	s_cbranch_execz .LBB0_878
	s_waitcnt lgkmcnt(0)
	v_readlane_b32 s12, v243, 7
	v_readlane_b32 s13, v243, 8
	v_mov_b32_e32 v1, 0
	s_add_u32 s12, s12, 0x3500
	s_addc_u32 s13, s13, 0
	global_load_dword v1, v1, s[12:13] sc1
	s_waitcnt vmcnt(0)
	v_cmp_eq_u32_e32 vcc, v1, v2
	s_and_saveexec_b64 s[8:9], vcc
	s_cbranch_execz .LBB0_877
	v_readlane_b32 s16, v243, 0
	v_readlane_b32 s17, v243, 1
	s_add_u32 s10, s16, 0x4200
	s_addc_u32 s11, s17, 0
	s_mov_b32 s24, 1
	s_mov_b64 s[14:15], 0
	v_mov_b32_e32 v1, 0
	v_readlane_b32 s18, v243, 2
	v_readlane_b32 s19, v243, 3
	s_branch .LBB0_868
